# P8: output bias as accumulator start value, next unit's bias loaded one epilogue ahead (no bias wait, no bias adds)
# baseline (speedup 1.0000x reference)
.LBB0_993:
	v_bfe_u32 v2, v178, 4, 2
	v_and_b32_e32 v0, 15, v178
	v_lshlrev_b32_e32 v1, 4, v2
	v_lshlrev_b32_e32 v3, 2, v178
	v_lshl_or_b32 v193, s11, 6, v0
	v_lshl_or_b32 v0, v0, 6, v1
	s_lshl_b32 s11, s11, 13
	v_and_b32_e32 v3, 32, v3
	v_bitop3_b32 v194, v0, s11, v3 bitop3:0xde
	s_lshl_b32 s11, s14, 5
	s_and_b32 s14, s11, 0x60
	v_lshlrev_b32_e32 v0, 6, v178
	s_movk_i32 s11, 0x3c0
	v_and_or_b32 v0, v0, s11, v1
	s_lshl_b32 s11, s14, 7
	s_add_u32 s16, s90, 0x191a0000
	s_addc_u32 s17, s91, 0
	s_add_u32 s18, s8, 0x4000
	s_addc_u32 s19, s9, 0
	s_add_i32 s52, s46, 0x8000
	v_bitop3_b32 v3, s11, v0, v3 bitop3:0xf6
	v_lshl_add_u64 v[0:1], s[18:19], 0, v[176:177]
	s_mov_b32 m0, s52
	s_add_i32 s53, s46, 0xa000
	s_waitcnt vmcnt(4)
	s_barrier
	global_load_lds_dwordx4 v[0:1], off
	v_lshl_add_u64 v[0:1], s[18:19], 0, v[180:181]
	s_add_u32 s18, s90, 0xf1a4000
	s_mov_b32 m0, s53
	s_addc_u32 s19, s91, 0
	global_load_lds_dwordx4 v[0:1], off
	s_add_i32 m0, s46, 0x18000
	v_lshl_add_u64 v[0:1], s[18:19], 0, v[184:185]
	global_load_lds_dwordx4 v[0:1], off
	s_add_i32 m0, s46, 0x1a000
	v_lshl_add_u64 v[0:1], s[18:19], 0, v[186:187]
	s_add_u32 s18, s8, 0x5000
	s_addc_u32 s19, s9, 0
	s_add_i32 s54, s46, 0xc000
	global_load_lds_dwordx4 v[0:1], off
	v_lshl_add_u64 v[0:1], s[18:19], 0, v[176:177]
	s_mov_b32 m0, s54
	s_add_i32 s55, s46, 0xe000
	global_load_lds_dwordx4 v[0:1], off
	v_lshl_add_u64 v[0:1], s[18:19], 0, v[180:181]
	s_mov_b32 m0, s55
	s_ashr_i32 s18, s33, 31
	global_load_lds_dwordx4 v[0:1], off
	s_lshr_b32 s18, s18, 29
	s_add_i32 s18, s33, s18
	s_ashr_i32 s19, s18, 3
	s_and_b32 s18, s18, -8
	s_sub_i32 s18, s33, s18
	s_ashr_i32 s20, s96, 3
	s_mul_i32 s18, s20, s18
	s_add_i32 s20, s18, s19
	s_cmp_lt_i32 s36, 24
	s_cselect_b64 s[18:19], -1, 0
	s_and_b64 s[2:3], s[2:3], exec
	s_mov_b32 s2, 0x20944
	s_cselect_b32 s56, s20, s33
	s_add_i32 s57, s2, 0x100
	s_mov_b32 s2, 0x20948
	s_add_i32 s58, s2, 0x100
	s_mov_b32 s2, 0x2094c
	s_add_i32 s59, s2, 0x100
	s_mov_b32 s2, 0x20950
	s_add_i32 s60, s2, 0x100
	s_mov_b32 s2, 0x20954
	s_add_i32 s61, s2, 0x100
	s_mov_b32 s2, 0x20958
	s_add_i32 s62, s2, 0x100
	s_mov_b32 s2, 0x2095c
	s_add_i32 s63, s2, 0x100
	s_mov_b32 s2, 0x20960
	s_add_i32 s64, s2, 0x100
	s_mov_b32 s2, 0x20964
	s_add_i32 s65, s2, 0x100
	s_mov_b32 s2, 0x20968
	s_add_i32 s68, s2, 0x100
	s_mov_b32 s2, 0x2096c
	s_add_i32 s69, s2, 0x100
	s_mov_b32 s2, 0x20970
	s_add_i32 s70, s2, 0x100
	s_mov_b32 s2, 0x20974
	s_addk_i32 s2, 0x100
	v_writelane_b32 v250, s2, 4
	s_mov_b32 s2, 0x20978
	s_addk_i32 s2, 0x100
	v_writelane_b32 v250, s2, 3
	s_mov_b32 s2, 0x2097c
	s_addk_i32 s2, 0x100
	v_writelane_b32 v250, s2, 5
	s_mov_b32 s2, 0x20980
	s_addk_i32 s2, 0x100
	v_writelane_b32 v250, s2, 6
	s_mov_b32 s2, 0x20984
	s_addk_i32 s2, 0x100
	v_writelane_b32 v250, s2, 7
	s_mov_b32 s2, 0x20988
	s_addk_i32 s2, 0x100
	v_writelane_b32 v250, s2, 8
	s_mov_b32 s2, 0x2098c
	s_addk_i32 s2, 0x100
	v_writelane_b32 v250, s2, 9
	s_mov_b32 s2, 0x20990
	s_addk_i32 s2, 0x100
	v_writelane_b32 v250, s2, 10
	s_mov_b32 s2, 0x20994
	s_addk_i32 s2, 0x100
	v_writelane_b32 v250, s2, 11
	s_mov_b32 s2, 0x20998
	s_addk_i32 s2, 0x100
	v_writelane_b32 v250, s2, 12
	s_mov_b32 s2, 0x2099c
	s_addk_i32 s2, 0x100
	v_writelane_b32 v250, s2, 13
	s_mov_b32 s2, 0x209a0
	s_addk_i32 s2, 0x100
	v_writelane_b32 v250, s2, 14
	s_mov_b32 s2, 0x209a4
	s_addk_i32 s2, 0x100
	v_writelane_b32 v250, s2, 15
	s_mov_b32 s2, 0x209a8
	s_add_i32 s84, s2, 0x100
	s_mov_b32 s2, 0x209ac
	s_add_i32 s85, s2, 0x100
	s_mov_b32 s2, 0x209b0
	s_add_i32 s97, s2, 0x100
	s_mov_b32 s2, 0x209b4
	s_waitcnt vmcnt(6)
	s_add_i32 s74, s2, 0x100
	s_mov_b32 s2, 0x209b8
	s_mov_b32 s11, 0x18000
	s_mov_b32 s15, 0
	v_lshlrev_b32_e32 v190, 2, v2
	s_add_i32 s73, s2, 0x100
	s_mov_b32 s2, 0x209bc
	v_mov_b32_e32 v191, v183
	v_or_b32_e32 v185, 16, v193
	v_or_b32_e32 v187, 32, v193
	v_or_b32_e32 v195, 48, v193
	s_add_i32 s75, s2, 0x100
	v_mov_b32_e32 v196, 0x7f7f7f7f
	v_mov_b32_e32 v197, 0x79797979
	s_add_i32 s76, s7, 0x100
	s_lshl_b32 s72, s14, 2
	v_lshlrev_b32_e32 v198, 2, v190
	s_mov_b32 s77, 0xc3e00000
	v_add_u32_e32 v199, 0x100, v3
	s_add_i32 s78, s11, 0x100
	v_mov_b32_e32 v200, 0x43e00000
	s_mov_b32 s44, s81
	s_mov_b32 s80, s15
	s_lshl_b32 s99, s6, 13
	s_lshl_b32 s100, s10, 2
	s_add_u32 s99, s99, s100
	s_add_u32 s99, s99, s72
	s_add_u32 s99, s99, s72
	s_add_u32 s100, s86, s99
	s_addc_u32 s101, s87, 0
	global_load_dwordx4 v[172:175], v198, s[100:101]
	global_load_dwordx4 v[168:171], v198, s[100:101] offset:64
	global_load_dwordx4 v[140:143], v198, s[100:101] offset:128
	global_load_dwordx4 v[136:139], v198, s[100:101] offset:192
	s_waitcnt vmcnt(0)
	v_mov_b32_e32 v164, v172
	v_mov_b32_e32 v165, v173
	v_mov_b32_e32 v166, v174
	v_mov_b32_e32 v167, v175
	v_mov_b32_e32 v160, v168
	v_mov_b32_e32 v161, v169
	v_mov_b32_e32 v162, v170
	v_mov_b32_e32 v163, v171
	v_mov_b32_e32 v156, v172
	v_mov_b32_e32 v157, v173
	v_mov_b32_e32 v158, v174
	v_mov_b32_e32 v159, v175
	v_mov_b32_e32 v152, v168
	v_mov_b32_e32 v153, v169
	v_mov_b32_e32 v154, v170
	v_mov_b32_e32 v155, v171
	v_mov_b32_e32 v148, v172
	v_mov_b32_e32 v149, v173
	v_mov_b32_e32 v150, v174
	v_mov_b32_e32 v151, v175
	v_mov_b32_e32 v144, v168
	v_mov_b32_e32 v145, v169
	v_mov_b32_e32 v146, v170
	v_mov_b32_e32 v147, v171
	v_mov_b32_e32 v132, v140
	v_mov_b32_e32 v133, v141
	v_mov_b32_e32 v134, v142
	v_mov_b32_e32 v135, v143
	v_mov_b32_e32 v128, v136
	v_mov_b32_e32 v129, v137
	v_mov_b32_e32 v130, v138
	v_mov_b32_e32 v131, v139
	v_mov_b32_e32 v124, v140
	v_mov_b32_e32 v125, v141
	v_mov_b32_e32 v126, v142
	v_mov_b32_e32 v127, v143
	v_mov_b32_e32 v120, v136
	v_mov_b32_e32 v121, v137
	v_mov_b32_e32 v122, v138
	v_mov_b32_e32 v123, v139
	v_mov_b32_e32 v116, v140
	v_mov_b32_e32 v117, v141
	v_mov_b32_e32 v118, v142
	v_mov_b32_e32 v119, v143
	v_mov_b32_e32 v112, v136
	v_mov_b32_e32 v113, v137
	v_mov_b32_e32 v114, v138
	v_mov_b32_e32 v115, v139
	v_mov_b32_e32 v108, v172
	v_mov_b32_e32 v109, v173
	v_mov_b32_e32 v110, v174
	v_mov_b32_e32 v111, v175
	v_mov_b32_e32 v104, v168
	v_mov_b32_e32 v105, v169
	v_mov_b32_e32 v106, v170
	v_mov_b32_e32 v107, v171
	v_mov_b32_e32 v100, v172
	v_mov_b32_e32 v101, v173
	v_mov_b32_e32 v102, v174
	v_mov_b32_e32 v103, v175
	v_mov_b32_e32 v96, v168
	v_mov_b32_e32 v97, v169
	v_mov_b32_e32 v98, v170
	v_mov_b32_e32 v99, v171
	v_mov_b32_e32 v92, v172
	v_mov_b32_e32 v93, v173
	v_mov_b32_e32 v94, v174
	v_mov_b32_e32 v95, v175
	v_mov_b32_e32 v88, v168
	v_mov_b32_e32 v89, v169
	v_mov_b32_e32 v90, v170
	v_mov_b32_e32 v91, v171
	v_mov_b32_e32 v84, v172
	v_mov_b32_e32 v85, v173
	v_mov_b32_e32 v86, v174
	v_mov_b32_e32 v87, v175
	v_mov_b32_e32 v80, v168
	v_mov_b32_e32 v81, v169
	v_mov_b32_e32 v82, v170
	v_mov_b32_e32 v83, v171
	v_mov_b32_e32 v76, v140
	v_mov_b32_e32 v77, v141
	v_mov_b32_e32 v78, v142
	v_mov_b32_e32 v79, v143
	v_mov_b32_e32 v72, v136
	v_mov_b32_e32 v73, v137
	v_mov_b32_e32 v74, v138
	v_mov_b32_e32 v75, v139
	v_mov_b32_e32 v68, v140
	v_mov_b32_e32 v69, v141
	v_mov_b32_e32 v70, v142
	v_mov_b32_e32 v71, v143
	v_mov_b32_e32 v64, v136
	v_mov_b32_e32 v65, v137
	v_mov_b32_e32 v66, v138
	v_mov_b32_e32 v67, v139
	v_mov_b32_e32 v60, v140
	v_mov_b32_e32 v61, v141
	v_mov_b32_e32 v62, v142
	v_mov_b32_e32 v63, v143
	v_mov_b32_e32 v56, v136
	v_mov_b32_e32 v57, v137
	v_mov_b32_e32 v58, v138
	v_mov_b32_e32 v59, v139
	v_mov_b32_e32 v52, v140
	v_mov_b32_e32 v53, v141
	v_mov_b32_e32 v54, v142
	v_mov_b32_e32 v55, v143
	v_mov_b32_e32 v48, v136
	v_mov_b32_e32 v49, v137
	v_mov_b32_e32 v50, v138
	v_mov_b32_e32 v51, v139
	s_barrier
	s_branch .LBB0_995

.LBB0_1047:
	s_andn2_b64 vcc, exec, s[24:25]
	s_ashr_i32 s11, s10, 31
	v_add_u32_e32 v16, s44, v193
	v_ashrrev_i32_e32 v17, 31, v16
	v_lshlrev_b64 v[252:253], 11, v[16:17]
	v_bfe_u32 v16, v178, 4, 2
	v_lshlrev_b32_e32 v16, 4, v16
	v_mov_b32_e32 v17, 0
	v_lshl_add_u64 v[252:253], s[16:17], 0, v[252:253]
	v_lshl_add_u64 v[252:253], v[252:253], 0, s[10:11]
	v_lshl_add_u64 v[252:253], v[252:253], 0, s[14:15]
	v_lshl_add_u64 v[252:253], v[252:253], 0, s[14:15]
	v_lshl_add_u64 v[252:253], v[252:253], 0, v[16:17]
	s_mov_b64 s[100:101], 0x8000
	v_med3_f32 v24, v172, s77, v200
	v_med3_f32 v25, v173, s77, v200
	v_med3_f32 v26, v174, s77, v200
	v_med3_f32 v27, v175, s77, v200
	v_med3_f32 v28, v168, s77, v200
	v_med3_f32 v29, v169, s77, v200
	v_med3_f32 v30, v170, s77, v200
	v_med3_f32 v31, v171, s77, v200
	v_med3_f32 v32, v140, s77, v200
	v_med3_f32 v33, v141, s77, v200
	v_med3_f32 v34, v142, s77, v200
	v_med3_f32 v35, v143, s77, v200
	v_med3_f32 v36, v136, s77, v200
	v_med3_f32 v37, v137, s77, v200
	v_med3_f32 v38, v138, s77, v200
	v_med3_f32 v39, v139, s77, v200
	s_lshl_b32 s99, s20, 13
	s_lshl_b32 s100, s21, 2
	s_add_u32 s99, s99, s100
	s_add_u32 s99, s99, s72
	s_add_u32 s99, s99, s72
	s_add_u32 s100, s86, s99
	s_addc_u32 s101, s87, 0
	global_load_dwordx4 v[172:175], v198, s[100:101]
	global_load_dwordx4 v[168:171], v198, s[100:101] offset:64
	global_load_dwordx4 v[140:143], v198, s[100:101] offset:128
	global_load_dwordx4 v[136:139], v198, s[100:101] offset:192
	s_mov_b64 s[100:101], 0x8000
	v_cvt_pk_fp8_f32 v20, v24, v25
	v_cvt_pk_fp8_f32 v21, v28, v29
	v_cvt_pk_fp8_f32 v22, v32, v33
	v_cvt_pk_fp8_f32 v23, v36, v37
	v_cvt_pk_fp8_f32 v20, v26, v27 op_sel:[0,0,1]
	v_cvt_pk_fp8_f32 v21, v30, v31 op_sel:[0,0,1]
	v_cvt_pk_fp8_f32 v22, v34, v35 op_sel:[0,0,1]
	v_cvt_pk_fp8_f32 v23, v38, v39 op_sel:[0,0,1]
	s_nop 1
	v_permlane32_swap_b32_e32 v20, v22
	v_permlane32_swap_b32_e32 v21, v23
	s_nop 1
	v_permlane16_swap_b32_e32 v20, v21
	v_permlane16_swap_b32_e32 v22, v23
	global_store_dwordx4 v[252:253], v[20:23], off
	v_lshl_add_u64 v[252:253], v[252:253], 0, s[100:101]
	v_med3_f32 v24, v164, s77, v200
	v_med3_f32 v25, v165, s77, v200
	v_med3_f32 v26, v166, s77, v200
	v_med3_f32 v27, v167, s77, v200
	v_med3_f32 v28, v160, s77, v200
	v_med3_f32 v29, v161, s77, v200
	v_med3_f32 v30, v162, s77, v200
	v_med3_f32 v31, v163, s77, v200
	v_med3_f32 v32, v132, s77, v200
	v_med3_f32 v33, v133, s77, v200
	v_med3_f32 v34, v134, s77, v200
	v_med3_f32 v35, v135, s77, v200
	v_med3_f32 v36, v128, s77, v200
	v_med3_f32 v37, v129, s77, v200
	v_med3_f32 v38, v130, s77, v200
	v_med3_f32 v39, v131, s77, v200
	v_cvt_pk_fp8_f32 v40, v24, v25
	v_cvt_pk_fp8_f32 v41, v28, v29
	v_cvt_pk_fp8_f32 v42, v32, v33
	v_cvt_pk_fp8_f32 v43, v36, v37
	v_cvt_pk_fp8_f32 v40, v26, v27 op_sel:[0,0,1]
	v_cvt_pk_fp8_f32 v41, v30, v31 op_sel:[0,0,1]
	v_cvt_pk_fp8_f32 v42, v34, v35 op_sel:[0,0,1]
	v_cvt_pk_fp8_f32 v43, v38, v39 op_sel:[0,0,1]
	s_nop 1
	v_permlane32_swap_b32_e32 v40, v42
	v_permlane32_swap_b32_e32 v41, v43
	s_nop 1
	v_permlane16_swap_b32_e32 v40, v41
	v_permlane16_swap_b32_e32 v42, v43
	global_store_dwordx4 v[252:253], v[40:43], off
	v_lshl_add_u64 v[252:253], v[252:253], 0, s[100:101]
	v_med3_f32 v24, v156, s77, v200
	v_med3_f32 v25, v157, s77, v200
	v_med3_f32 v26, v158, s77, v200
	v_med3_f32 v27, v159, s77, v200
	v_med3_f32 v28, v152, s77, v200
	v_med3_f32 v29, v153, s77, v200
	v_med3_f32 v30, v154, s77, v200
	v_med3_f32 v31, v155, s77, v200
	v_med3_f32 v32, v124, s77, v200
	v_med3_f32 v33, v125, s77, v200
	v_med3_f32 v34, v126, s77, v200
	v_med3_f32 v35, v127, s77, v200
	v_med3_f32 v36, v120, s77, v200
	v_med3_f32 v37, v121, s77, v200
	v_med3_f32 v38, v122, s77, v200
	v_med3_f32 v39, v123, s77, v200
	v_cvt_pk_fp8_f32 v20, v24, v25
	v_cvt_pk_fp8_f32 v21, v28, v29
	v_cvt_pk_fp8_f32 v22, v32, v33
	v_cvt_pk_fp8_f32 v23, v36, v37
	v_cvt_pk_fp8_f32 v20, v26, v27 op_sel:[0,0,1]
	v_cvt_pk_fp8_f32 v21, v30, v31 op_sel:[0,0,1]
	v_cvt_pk_fp8_f32 v22, v34, v35 op_sel:[0,0,1]
	v_cvt_pk_fp8_f32 v23, v38, v39 op_sel:[0,0,1]
	s_nop 1
	v_permlane32_swap_b32_e32 v20, v22
	v_permlane32_swap_b32_e32 v21, v23
	s_nop 1
	v_permlane16_swap_b32_e32 v20, v21
	v_permlane16_swap_b32_e32 v22, v23
	global_store_dwordx4 v[252:253], v[20:23], off
	v_lshl_add_u64 v[252:253], v[252:253], 0, s[100:101]
	v_med3_f32 v24, v148, s77, v200
	v_med3_f32 v25, v149, s77, v200
	v_med3_f32 v26, v150, s77, v200
	v_med3_f32 v27, v151, s77, v200
	v_med3_f32 v28, v144, s77, v200
	v_med3_f32 v29, v145, s77, v200
	v_med3_f32 v30, v146, s77, v200
	v_med3_f32 v31, v147, s77, v200
	v_med3_f32 v32, v116, s77, v200
	v_med3_f32 v33, v117, s77, v200
	v_med3_f32 v34, v118, s77, v200
	v_med3_f32 v35, v119, s77, v200
	v_med3_f32 v36, v112, s77, v200
	v_med3_f32 v37, v113, s77, v200
	v_med3_f32 v38, v114, s77, v200
	v_med3_f32 v39, v115, s77, v200
	v_cvt_pk_fp8_f32 v40, v24, v25
	v_cvt_pk_fp8_f32 v41, v28, v29
	v_cvt_pk_fp8_f32 v42, v32, v33
	v_cvt_pk_fp8_f32 v43, v36, v37
	v_cvt_pk_fp8_f32 v40, v26, v27 op_sel:[0,0,1]
	v_cvt_pk_fp8_f32 v41, v30, v31 op_sel:[0,0,1]
	v_cvt_pk_fp8_f32 v42, v34, v35 op_sel:[0,0,1]
	v_cvt_pk_fp8_f32 v43, v38, v39 op_sel:[0,0,1]
	s_nop 1
	v_permlane32_swap_b32_e32 v40, v42
	v_permlane32_swap_b32_e32 v41, v43
	s_nop 1
	v_permlane16_swap_b32_e32 v40, v41
	v_permlane16_swap_b32_e32 v42, v43
	global_store_dwordx4 v[252:253], v[40:43], off
	s_mov_b64 s[100:101], 0x28000
	v_lshl_add_u64 v[252:253], v[252:253], 0, s[100:101]
	s_mov_b64 s[100:101], 0x8000
	v_med3_f32 v24, v108, s77, v200
	v_med3_f32 v25, v109, s77, v200
	v_med3_f32 v26, v110, s77, v200
	v_med3_f32 v27, v111, s77, v200
	v_med3_f32 v28, v104, s77, v200
	v_med3_f32 v29, v105, s77, v200
	v_med3_f32 v30, v106, s77, v200
	v_med3_f32 v31, v107, s77, v200
	v_med3_f32 v32, v76, s77, v200
	v_med3_f32 v33, v77, s77, v200
	v_med3_f32 v34, v78, s77, v200
	v_med3_f32 v35, v79, s77, v200
	v_med3_f32 v36, v72, s77, v200
	v_med3_f32 v37, v73, s77, v200
	v_med3_f32 v38, v74, s77, v200
	v_med3_f32 v39, v75, s77, v200
	v_cvt_pk_fp8_f32 v20, v24, v25
	v_cvt_pk_fp8_f32 v21, v28, v29
	v_cvt_pk_fp8_f32 v22, v32, v33
	v_cvt_pk_fp8_f32 v23, v36, v37
	v_cvt_pk_fp8_f32 v20, v26, v27 op_sel:[0,0,1]
	v_cvt_pk_fp8_f32 v21, v30, v31 op_sel:[0,0,1]
	v_cvt_pk_fp8_f32 v22, v34, v35 op_sel:[0,0,1]
	v_cvt_pk_fp8_f32 v23, v38, v39 op_sel:[0,0,1]
	s_nop 1
	v_permlane32_swap_b32_e32 v20, v22
	v_permlane32_swap_b32_e32 v21, v23
	s_nop 1
	v_permlane16_swap_b32_e32 v20, v21
	v_permlane16_swap_b32_e32 v22, v23
	global_store_dwordx4 v[252:253], v[20:23], off
	v_lshl_add_u64 v[252:253], v[252:253], 0, s[100:101]
	v_med3_f32 v24, v100, s77, v200
	v_med3_f32 v25, v101, s77, v200
	v_med3_f32 v26, v102, s77, v200
	v_med3_f32 v27, v103, s77, v200
	v_med3_f32 v28, v96, s77, v200
	v_med3_f32 v29, v97, s77, v200
	v_med3_f32 v30, v98, s77, v200
	v_med3_f32 v31, v99, s77, v200
	v_med3_f32 v32, v68, s77, v200
	v_med3_f32 v33, v69, s77, v200
	v_med3_f32 v34, v70, s77, v200
	v_med3_f32 v35, v71, s77, v200
	v_med3_f32 v36, v64, s77, v200
	v_med3_f32 v37, v65, s77, v200
	v_med3_f32 v38, v66, s77, v200
	v_med3_f32 v39, v67, s77, v200
	v_cvt_pk_fp8_f32 v40, v24, v25
	v_cvt_pk_fp8_f32 v41, v28, v29
	v_cvt_pk_fp8_f32 v42, v32, v33
	v_cvt_pk_fp8_f32 v43, v36, v37
	v_cvt_pk_fp8_f32 v40, v26, v27 op_sel:[0,0,1]
	v_cvt_pk_fp8_f32 v41, v30, v31 op_sel:[0,0,1]
	v_cvt_pk_fp8_f32 v42, v34, v35 op_sel:[0,0,1]
	v_cvt_pk_fp8_f32 v43, v38, v39 op_sel:[0,0,1]
	s_nop 1
	v_permlane32_swap_b32_e32 v40, v42
	v_permlane32_swap_b32_e32 v41, v43
	s_nop 1
	v_permlane16_swap_b32_e32 v40, v41
	v_permlane16_swap_b32_e32 v42, v43
	global_store_dwordx4 v[252:253], v[40:43], off
	v_lshl_add_u64 v[252:253], v[252:253], 0, s[100:101]
	v_med3_f32 v24, v92, s77, v200
	v_med3_f32 v25, v93, s77, v200
	v_med3_f32 v26, v94, s77, v200
	v_med3_f32 v27, v95, s77, v200
	v_med3_f32 v28, v88, s77, v200
	v_med3_f32 v29, v89, s77, v200
	v_med3_f32 v30, v90, s77, v200
	v_med3_f32 v31, v91, s77, v200
	v_med3_f32 v32, v60, s77, v200
	v_med3_f32 v33, v61, s77, v200
	v_med3_f32 v34, v62, s77, v200
	v_med3_f32 v35, v63, s77, v200
	v_med3_f32 v36, v56, s77, v200
	v_med3_f32 v37, v57, s77, v200
	v_med3_f32 v38, v58, s77, v200
	v_med3_f32 v39, v59, s77, v200
	v_cvt_pk_fp8_f32 v20, v24, v25
	v_cvt_pk_fp8_f32 v21, v28, v29
	v_cvt_pk_fp8_f32 v22, v32, v33
	v_cvt_pk_fp8_f32 v23, v36, v37
	v_cvt_pk_fp8_f32 v20, v26, v27 op_sel:[0,0,1]
	v_cvt_pk_fp8_f32 v21, v30, v31 op_sel:[0,0,1]
	v_cvt_pk_fp8_f32 v22, v34, v35 op_sel:[0,0,1]
	v_cvt_pk_fp8_f32 v23, v38, v39 op_sel:[0,0,1]
	s_nop 1
	v_permlane32_swap_b32_e32 v20, v22
	v_permlane32_swap_b32_e32 v21, v23
	s_nop 1
	v_permlane16_swap_b32_e32 v20, v21
	v_permlane16_swap_b32_e32 v22, v23
	global_store_dwordx4 v[252:253], v[20:23], off
	v_lshl_add_u64 v[252:253], v[252:253], 0, s[100:101]
	v_med3_f32 v24, v84, s77, v200
	v_med3_f32 v25, v85, s77, v200
	v_med3_f32 v26, v86, s77, v200
	v_med3_f32 v27, v87, s77, v200
	v_med3_f32 v28, v80, s77, v200
	v_med3_f32 v29, v81, s77, v200
	v_med3_f32 v30, v82, s77, v200
	v_med3_f32 v31, v83, s77, v200
	v_med3_f32 v32, v52, s77, v200
	v_med3_f32 v33, v53, s77, v200
	v_med3_f32 v34, v54, s77, v200
	v_med3_f32 v35, v55, s77, v200
	v_med3_f32 v36, v48, s77, v200
	v_med3_f32 v37, v49, s77, v200
	v_med3_f32 v38, v50, s77, v200
	v_med3_f32 v39, v51, s77, v200
	v_cvt_pk_fp8_f32 v40, v24, v25
	v_cvt_pk_fp8_f32 v41, v28, v29
	v_cvt_pk_fp8_f32 v42, v32, v33
	v_cvt_pk_fp8_f32 v43, v36, v37
	v_cvt_pk_fp8_f32 v40, v26, v27 op_sel:[0,0,1]
	v_cvt_pk_fp8_f32 v41, v30, v31 op_sel:[0,0,1]
	v_cvt_pk_fp8_f32 v42, v34, v35 op_sel:[0,0,1]
	v_cvt_pk_fp8_f32 v43, v38, v39 op_sel:[0,0,1]
	s_nop 1
	v_permlane32_swap_b32_e32 v40, v42
	v_permlane32_swap_b32_e32 v41, v43
	s_nop 1
	v_permlane16_swap_b32_e32 v40, v41
	v_permlane16_swap_b32_e32 v42, v43
	global_store_dwordx4 v[252:253], v[40:43], off
	s_cbranch_vccnz .LBB0_994
	s_mov_b32 s81, s79
	s_mov_b64 s[8:9], s[22:23]
	s_mov_b32 s6, s20
	s_mov_b32 s44, s82
	s_mov_b32 s10, s21
	s_mov_b32 s80, s71
	s_waitcnt vmcnt(8)
	v_mov_b32_e32 v164, v172
	v_mov_b32_e32 v165, v173
	v_mov_b32_e32 v166, v174
	v_mov_b32_e32 v167, v175
	v_mov_b32_e32 v160, v168
	v_mov_b32_e32 v161, v169
	v_mov_b32_e32 v162, v170
	v_mov_b32_e32 v163, v171
	v_mov_b32_e32 v156, v172
	v_mov_b32_e32 v157, v173
	v_mov_b32_e32 v158, v174
	v_mov_b32_e32 v159, v175
	v_mov_b32_e32 v152, v168
	v_mov_b32_e32 v153, v169
	v_mov_b32_e32 v154, v170
	v_mov_b32_e32 v155, v171
	v_mov_b32_e32 v148, v172
	v_mov_b32_e32 v149, v173
	v_mov_b32_e32 v150, v174
	v_mov_b32_e32 v151, v175
	v_mov_b32_e32 v144, v168
	v_mov_b32_e32 v145, v169
	v_mov_b32_e32 v146, v170
	v_mov_b32_e32 v147, v171
	v_mov_b32_e32 v132, v140
	v_mov_b32_e32 v133, v141
	v_mov_b32_e32 v134, v142
	v_mov_b32_e32 v135, v143
	v_mov_b32_e32 v128, v136
	v_mov_b32_e32 v129, v137
	v_mov_b32_e32 v130, v138
	v_mov_b32_e32 v131, v139
	v_mov_b32_e32 v124, v140
	v_mov_b32_e32 v125, v141
	v_mov_b32_e32 v126, v142
	v_mov_b32_e32 v127, v143
	v_mov_b32_e32 v120, v136
	v_mov_b32_e32 v121, v137
	v_mov_b32_e32 v122, v138
	v_mov_b32_e32 v123, v139
	v_mov_b32_e32 v116, v140
	v_mov_b32_e32 v117, v141
	v_mov_b32_e32 v118, v142
	v_mov_b32_e32 v119, v143
	v_mov_b32_e32 v112, v136
	v_mov_b32_e32 v113, v137
	v_mov_b32_e32 v114, v138
	v_mov_b32_e32 v115, v139
	v_mov_b32_e32 v108, v172
	v_mov_b32_e32 v109, v173
	v_mov_b32_e32 v110, v174
	v_mov_b32_e32 v111, v175
	v_mov_b32_e32 v104, v168
	v_mov_b32_e32 v105, v169
	v_mov_b32_e32 v106, v170
	v_mov_b32_e32 v107, v171
	v_mov_b32_e32 v100, v172
	v_mov_b32_e32 v101, v173
	v_mov_b32_e32 v102, v174
	v_mov_b32_e32 v103, v175
	v_mov_b32_e32 v96, v168
	v_mov_b32_e32 v97, v169
	v_mov_b32_e32 v98, v170
	v_mov_b32_e32 v99, v171
	v_mov_b32_e32 v92, v172
	v_mov_b32_e32 v93, v173
	v_mov_b32_e32 v94, v174
	v_mov_b32_e32 v95, v175
	v_mov_b32_e32 v88, v168
	v_mov_b32_e32 v89, v169
	v_mov_b32_e32 v90, v170
	v_mov_b32_e32 v91, v171
	v_mov_b32_e32 v84, v172
	v_mov_b32_e32 v85, v173
	v_mov_b32_e32 v86, v174
	v_mov_b32_e32 v87, v175
	v_mov_b32_e32 v80, v168
	v_mov_b32_e32 v81, v169
	v_mov_b32_e32 v82, v170
	v_mov_b32_e32 v83, v171
	v_mov_b32_e32 v76, v140
	v_mov_b32_e32 v77, v141
	v_mov_b32_e32 v78, v142
	v_mov_b32_e32 v79, v143
	v_mov_b32_e32 v72, v136
	v_mov_b32_e32 v73, v137
	v_mov_b32_e32 v74, v138
	v_mov_b32_e32 v75, v139
	v_mov_b32_e32 v68, v140
	v_mov_b32_e32 v69, v141
	v_mov_b32_e32 v70, v142
	v_mov_b32_e32 v71, v143
	v_mov_b32_e32 v64, v136
	v_mov_b32_e32 v65, v137
	v_mov_b32_e32 v66, v138
	v_mov_b32_e32 v67, v139
	v_mov_b32_e32 v60, v140
	v_mov_b32_e32 v61, v141
	v_mov_b32_e32 v62, v142
	v_mov_b32_e32 v63, v143
	v_mov_b32_e32 v56, v136
	v_mov_b32_e32 v57, v137
	v_mov_b32_e32 v58, v138
	v_mov_b32_e32 v59, v139
	v_mov_b32_e32 v52, v140
	v_mov_b32_e32 v53, v141
	v_mov_b32_e32 v54, v142
	v_mov_b32_e32 v55, v143
	v_mov_b32_e32 v48, v136
	v_mov_b32_e32 v49, v137
	v_mov_b32_e32 v50, v138
	v_mov_b32_e32 v51, v139
	s_branch .LBB0_994
